# v77 stack + routing top-8 rounds: wave max across rows/halves via v_permlane16/32_swap instead of two ds_bpermute round trips per round
# speedup vs baseline: 1.0060x; 1.0060x over previous
.LBB0_585:
	s_or_b64 exec, exec, s[28:29]
	v_cmp_gt_f32_e32 vcc, v9, v20
	v_cndmask_b32_e64 v18, 0, 1, s[2:3]
	s_mov_b32 s2, 0xff800000
	v_cndmask_b32_e64 v9, 0, 1, vcc
	v_cmp_gt_f32_e32 vcc, v38, v20
	s_nop 1
	v_addc_co_u32_e32 v9, vcc, v9, v18, vcc
	v_cmp_gt_f32_e32 vcc, v0, v20
	s_nop 1
	v_cndmask_b32_e64 v0, 0, 1, vcc
	v_cmp_gt_f32_e32 vcc, v37, v20
	s_nop 1
	v_addc_co_u32_e32 v0, vcc, v9, v0, vcc
	v_cmp_gt_f32_e32 vcc, v39, v20
	s_nop 1
	v_cndmask_b32_e64 v9, 0, 1, vcc
	v_cmp_gt_f32_e32 vcc, v21, v20
	s_nop 1
	v_addc_co_u32_e32 v9, vcc, v0, v9, vcc
	v_mov_b32_e32 v0, s2
	v_cmp_gt_u32_e32 vcc, 4, v9
	s_nop 1
	v_cndmask_b32_e32 v9, v0, v14, vcc
	v_cndmask_b32_e32 v0, v17, v17, vcc
	v_cndmask_b32_e32 v16, v16, v16, vcc
	v_cndmask_b32_e32 v14, v15, v15, vcc
	v_cmp_gt_u32_e32 vcc, 4, v36
	s_nop 1
	v_cndmask_b32_e32 v14, v26, v14, vcc
	v_cmp_gt_u32_e32 vcc, 4, v35
	s_nop 1
	v_cndmask_b32_e32 v15, v26, v16, vcc
	v_cmp_gt_u32_e32 vcc, 4, v33
	v_max_f32_e32 v17, v15, v15
	s_nop 0
	v_cndmask_b32_e32 v0, v26, v0, vcc
	v_max_f32_e32 v16, v0, v0
	v_max_f32_e32 v16, v17, v16
	v_max3_f32 v16, v9, v14, v16
	s_nop 1
	v_mov_b32_dpp v17, v16 quad_perm:[1,0,3,2] row_mask:0xf bank_mask:0xf bound_ctrl:1
	v_max_f32_e32 v17, v17, v17
	v_max_f32_e32 v16, v16, v17
	s_nop 1
	v_mov_b32_dpp v17, v16 quad_perm:[2,3,0,1] row_mask:0xf bank_mask:0xf bound_ctrl:1
	v_max_f32_e32 v17, v17, v17
	v_max_f32_e32 v16, v16, v17
	s_nop 1
	v_mov_b32_dpp v17, v16 row_half_mirror row_mask:0xf bank_mask:0xf bound_ctrl:1
	v_max_f32_e32 v17, v17, v17
	v_max_f32_e32 v16, v16, v17
	s_nop 1
	v_mov_b32_dpp v17, v16 row_mirror row_mask:0xf bank_mask:0xf bound_ctrl:1
	v_max_f32_e32 v17, v17, v17
	v_max_f32_e32 v16, v16, v17
	v_mov_b32_e32 v17, v16
	v_mov_b32_e32 v60, v16
	s_nop 1
	v_permlane16_swap_b32 v17, v60
	v_max_f32_e32 v16, v17, v60
	v_mov_b32_e32 v17, v16
	v_mov_b32_e32 v60, v16
	s_nop 1
	v_permlane32_swap_b32 v17, v60
	v_max_f32_e32 v16, v17, v60
	v_cmp_eq_f32_e32 vcc, v9, v16
	v_cmp_eq_f32_e64 s[28:29], v14, v16
	v_cmp_eq_f32_e64 s[2:3], v15, v16
	v_cmp_eq_f32_e64 s[48:49], v0, v16
	s_cbranch_vccz .LBB0_587
	s_ff1_i32_b64 s56, vcc
	s_cbranch_execz .LBB0_588
	s_branch .LBB0_594

.LBB0_594:
	s_and_b32 s2, s56, 63
	s_lshr_b32 s28, s56, 6
	s_cmp_lt_u32 s56, 64
	v_cmp_eq_u32_e32 vcc, s2, v22
	s_cselect_b64 s[2:3], -1, 0
	s_and_b64 s[2:3], s[2:3], vcc
	s_cmp_eq_u32 s28, 1
	v_cndmask_b32_e64 v9, v9, v26, s[2:3]
	s_cselect_b64 s[2:3], -1, 0
	s_and_b64 s[2:3], vcc, s[2:3]
	s_cmp_eq_u32 s28, 2
	v_cndmask_b32_e64 v14, v14, v26, s[2:3]
	s_cselect_b64 s[2:3], -1, 0
	s_and_b64 s[2:3], vcc, s[2:3]
	s_cmp_eq_u32 s28, 3
	v_cndmask_b32_e64 v15, v15, v26, s[2:3]
	s_cselect_b64 s[2:3], -1, 0
	s_and_b64 vcc, vcc, s[2:3]
	v_cndmask_b32_e32 v0, v0, v26, vcc
	v_max_f32_e32 v16, v0, v0
	v_max_f32_e32 v17, v15, v15
	v_max_f32_e32 v16, v17, v16
	v_max3_f32 v16, v9, v14, v16
	s_nop 1
	v_mov_b32_dpp v17, v16 quad_perm:[1,0,3,2] row_mask:0xf bank_mask:0xf bound_ctrl:1
	v_max_f32_e32 v17, v17, v17
	v_max_f32_e32 v16, v16, v17
	s_nop 1
	v_mov_b32_dpp v17, v16 quad_perm:[2,3,0,1] row_mask:0xf bank_mask:0xf bound_ctrl:1
	v_max_f32_e32 v17, v17, v17
	v_max_f32_e32 v16, v16, v17
	s_nop 1
	v_mov_b32_dpp v17, v16 row_half_mirror row_mask:0xf bank_mask:0xf bound_ctrl:1
	v_max_f32_e32 v17, v17, v17
	v_max_f32_e32 v16, v16, v17
	s_nop 1
	v_mov_b32_dpp v17, v16 row_mirror row_mask:0xf bank_mask:0xf bound_ctrl:1
	v_max_f32_e32 v17, v17, v17
	v_max_f32_e32 v16, v16, v17
	v_mov_b32_e32 v17, v16
	v_mov_b32_e32 v60, v16
	s_nop 1
	v_permlane16_swap_b32 v17, v60
	v_max_f32_e32 v16, v17, v60
	v_mov_b32_e32 v17, v16
	v_mov_b32_e32 v60, v16
	s_nop 1
	v_permlane32_swap_b32 v17, v60
	v_max_f32_e32 v16, v17, v60
	v_cmp_eq_f32_e32 vcc, v9, v16
	v_cmp_eq_f32_e64 s[28:29], v14, v16
	v_cmp_eq_f32_e64 s[2:3], v15, v16
	v_cmp_eq_f32_e64 s[48:49], v0, v16
	s_cbranch_vccz .LBB0_596
	s_ff1_i32_b64 s57, vcc
	s_cbranch_execz .LBB0_597
	s_branch .LBB0_603

.LBB0_603:
	s_and_b32 s2, s57, 63
	s_lshr_b32 s28, s57, 6
	s_cmp_lt_u32 s57, 64
	v_cmp_eq_u32_e32 vcc, s2, v22
	s_cselect_b64 s[2:3], -1, 0
	s_and_b64 s[2:3], s[2:3], vcc
	s_cmp_eq_u32 s28, 1
	v_cndmask_b32_e64 v9, v9, v26, s[2:3]
	s_cselect_b64 s[2:3], -1, 0
	s_and_b64 s[2:3], vcc, s[2:3]
	s_cmp_eq_u32 s28, 2
	v_cndmask_b32_e64 v14, v14, v26, s[2:3]
	s_cselect_b64 s[2:3], -1, 0
	s_and_b64 s[2:3], vcc, s[2:3]
	s_cmp_eq_u32 s28, 3
	v_cndmask_b32_e64 v15, v15, v26, s[2:3]
	s_cselect_b64 s[2:3], -1, 0
	s_and_b64 vcc, vcc, s[2:3]
	v_cndmask_b32_e32 v0, v0, v26, vcc
	v_max_f32_e32 v16, v0, v0
	v_max_f32_e32 v17, v15, v15
	v_max_f32_e32 v16, v17, v16
	v_max3_f32 v16, v9, v14, v16
	s_nop 1
	v_mov_b32_dpp v17, v16 quad_perm:[1,0,3,2] row_mask:0xf bank_mask:0xf bound_ctrl:1
	v_max_f32_e32 v17, v17, v17
	v_max_f32_e32 v16, v16, v17
	s_nop 1
	v_mov_b32_dpp v17, v16 quad_perm:[2,3,0,1] row_mask:0xf bank_mask:0xf bound_ctrl:1
	v_max_f32_e32 v17, v17, v17
	v_max_f32_e32 v16, v16, v17
	s_nop 1
	v_mov_b32_dpp v17, v16 row_half_mirror row_mask:0xf bank_mask:0xf bound_ctrl:1
	v_max_f32_e32 v17, v17, v17
	v_max_f32_e32 v16, v16, v17
	s_nop 1
	v_mov_b32_dpp v17, v16 row_mirror row_mask:0xf bank_mask:0xf bound_ctrl:1
	v_max_f32_e32 v17, v17, v17
	v_max_f32_e32 v16, v16, v17
	v_mov_b32_e32 v17, v16
	v_mov_b32_e32 v60, v16
	s_nop 1
	v_permlane16_swap_b32 v17, v60
	v_max_f32_e32 v16, v17, v60
	v_mov_b32_e32 v17, v16
	v_mov_b32_e32 v60, v16
	s_nop 1
	v_permlane32_swap_b32 v17, v60
	v_max_f32_e32 v16, v17, v60
	v_cmp_eq_f32_e32 vcc, v9, v16
	v_cmp_eq_f32_e64 s[28:29], v14, v16
	v_cmp_eq_f32_e64 s[2:3], v15, v16
	v_cmp_eq_f32_e64 s[48:49], v0, v16
	s_cbranch_vccz .LBB0_605
	s_ff1_i32_b64 s58, vcc
	s_cbranch_execz .LBB0_606
	s_branch .LBB0_612

.LBB0_612:
	s_and_b32 s2, s58, 63
	s_lshr_b32 s28, s58, 6
	s_cmp_lt_u32 s58, 64
	v_cmp_eq_u32_e32 vcc, s2, v22
	s_cselect_b64 s[2:3], -1, 0
	s_and_b64 s[2:3], s[2:3], vcc
	s_cmp_eq_u32 s28, 1
	v_cndmask_b32_e64 v9, v9, v26, s[2:3]
	s_cselect_b64 s[2:3], -1, 0
	s_and_b64 s[2:3], vcc, s[2:3]
	s_cmp_eq_u32 s28, 2
	v_cndmask_b32_e64 v14, v14, v26, s[2:3]
	s_cselect_b64 s[2:3], -1, 0
	s_and_b64 s[2:3], vcc, s[2:3]
	s_cmp_eq_u32 s28, 3
	v_cndmask_b32_e64 v15, v15, v26, s[2:3]
	s_cselect_b64 s[2:3], -1, 0
	s_and_b64 vcc, vcc, s[2:3]
	v_cndmask_b32_e32 v0, v0, v26, vcc
	v_max_f32_e32 v16, v0, v0
	v_max_f32_e32 v17, v15, v15
	v_max_f32_e32 v16, v17, v16
	v_max3_f32 v16, v9, v14, v16
	s_nop 1
	v_mov_b32_dpp v17, v16 quad_perm:[1,0,3,2] row_mask:0xf bank_mask:0xf bound_ctrl:1
	v_max_f32_e32 v17, v17, v17
	v_max_f32_e32 v16, v16, v17
	s_nop 1
	v_mov_b32_dpp v17, v16 quad_perm:[2,3,0,1] row_mask:0xf bank_mask:0xf bound_ctrl:1
	v_max_f32_e32 v17, v17, v17
	v_max_f32_e32 v16, v16, v17
	s_nop 1
	v_mov_b32_dpp v17, v16 row_half_mirror row_mask:0xf bank_mask:0xf bound_ctrl:1
	v_max_f32_e32 v17, v17, v17
	v_max_f32_e32 v16, v16, v17
	s_nop 1
	v_mov_b32_dpp v17, v16 row_mirror row_mask:0xf bank_mask:0xf bound_ctrl:1
	v_max_f32_e32 v17, v17, v17
	v_max_f32_e32 v16, v16, v17
	v_mov_b32_e32 v17, v16
	v_mov_b32_e32 v60, v16
	s_nop 1
	v_permlane16_swap_b32 v17, v60
	v_max_f32_e32 v16, v17, v60
	v_mov_b32_e32 v17, v16
	v_mov_b32_e32 v60, v16
	s_nop 1
	v_permlane32_swap_b32 v17, v60
	v_max_f32_e32 v16, v17, v60
	v_cmp_eq_f32_e32 vcc, v9, v16
	v_cmp_eq_f32_e64 s[28:29], v14, v16
	v_cmp_eq_f32_e64 s[2:3], v15, v16
	v_cmp_eq_f32_e64 s[48:49], v0, v16
	s_cbranch_vccz .LBB0_614
	s_ff1_i32_b64 s59, vcc
	s_cbranch_execz .LBB0_615
	s_branch .LBB0_621

.LBB0_621:
	s_and_b32 s2, s59, 63
	s_lshr_b32 s28, s59, 6
	s_cmp_lt_u32 s59, 64
	v_cmp_eq_u32_e32 vcc, s2, v22
	s_cselect_b64 s[2:3], -1, 0
	s_and_b64 s[2:3], s[2:3], vcc
	s_cmp_eq_u32 s28, 1
	v_cndmask_b32_e64 v9, v9, v26, s[2:3]
	s_cselect_b64 s[2:3], -1, 0
	s_and_b64 s[2:3], vcc, s[2:3]
	s_cmp_eq_u32 s28, 2
	v_cndmask_b32_e64 v14, v14, v26, s[2:3]
	s_cselect_b64 s[2:3], -1, 0
	s_and_b64 s[2:3], vcc, s[2:3]
	s_cmp_eq_u32 s28, 3
	v_cndmask_b32_e64 v15, v15, v26, s[2:3]
	s_cselect_b64 s[2:3], -1, 0
	s_and_b64 vcc, vcc, s[2:3]
	v_cndmask_b32_e32 v0, v0, v26, vcc
	v_max_f32_e32 v16, v0, v0
	v_max_f32_e32 v17, v15, v15
	v_max_f32_e32 v16, v17, v16
	v_max3_f32 v16, v9, v14, v16
	s_nop 1
	v_mov_b32_dpp v17, v16 quad_perm:[1,0,3,2] row_mask:0xf bank_mask:0xf bound_ctrl:1
	v_max_f32_e32 v17, v17, v17
	v_max_f32_e32 v16, v16, v17
	s_nop 1
	v_mov_b32_dpp v17, v16 quad_perm:[2,3,0,1] row_mask:0xf bank_mask:0xf bound_ctrl:1
	v_max_f32_e32 v17, v17, v17
	v_max_f32_e32 v16, v16, v17
	s_nop 1
	v_mov_b32_dpp v17, v16 row_half_mirror row_mask:0xf bank_mask:0xf bound_ctrl:1
	v_max_f32_e32 v17, v17, v17
	v_max_f32_e32 v16, v16, v17
	s_nop 1
	v_mov_b32_dpp v17, v16 row_mirror row_mask:0xf bank_mask:0xf bound_ctrl:1
	v_max_f32_e32 v17, v17, v17
	v_max_f32_e32 v16, v16, v17
	v_mov_b32_e32 v17, v16
	v_mov_b32_e32 v60, v16
	s_nop 1
	v_permlane16_swap_b32 v17, v60
	v_max_f32_e32 v16, v17, v60
	v_mov_b32_e32 v17, v16
	v_mov_b32_e32 v60, v16
	s_nop 1
	v_permlane32_swap_b32 v17, v60
	v_max_f32_e32 v16, v17, v60
	v_cmp_eq_f32_e32 vcc, v9, v16
	v_cmp_eq_f32_e64 s[28:29], v14, v16
	v_cmp_eq_f32_e64 s[2:3], v15, v16
	v_cmp_eq_f32_e64 s[48:49], v0, v16
	s_cbranch_vccz .LBB0_623
	s_ff1_i32_b64 s60, vcc
	s_cbranch_execz .LBB0_624
	s_branch .LBB0_630

.LBB0_630:
	s_and_b32 s2, s60, 63
	s_lshr_b32 s28, s60, 6
	s_cmp_lt_u32 s60, 64
	v_cmp_eq_u32_e32 vcc, s2, v22
	s_cselect_b64 s[2:3], -1, 0
	s_and_b64 s[2:3], s[2:3], vcc
	s_cmp_eq_u32 s28, 1
	v_cndmask_b32_e64 v9, v9, v26, s[2:3]
	s_cselect_b64 s[2:3], -1, 0
	s_and_b64 s[2:3], vcc, s[2:3]
	s_cmp_eq_u32 s28, 2
	v_cndmask_b32_e64 v14, v14, v26, s[2:3]
	s_cselect_b64 s[2:3], -1, 0
	s_and_b64 s[2:3], vcc, s[2:3]
	s_cmp_eq_u32 s28, 3
	v_cndmask_b32_e64 v15, v15, v26, s[2:3]
	s_cselect_b64 s[2:3], -1, 0
	s_and_b64 vcc, vcc, s[2:3]
	v_cndmask_b32_e32 v0, v0, v26, vcc
	v_max_f32_e32 v16, v0, v0
	v_max_f32_e32 v17, v15, v15
	v_max_f32_e32 v16, v17, v16
	v_max3_f32 v16, v9, v14, v16
	s_nop 1
	v_mov_b32_dpp v17, v16 quad_perm:[1,0,3,2] row_mask:0xf bank_mask:0xf bound_ctrl:1
	v_max_f32_e32 v17, v17, v17
	v_max_f32_e32 v16, v16, v17
	s_nop 1
	v_mov_b32_dpp v17, v16 quad_perm:[2,3,0,1] row_mask:0xf bank_mask:0xf bound_ctrl:1
	v_max_f32_e32 v17, v17, v17
	v_max_f32_e32 v16, v16, v17
	s_nop 1
	v_mov_b32_dpp v17, v16 row_half_mirror row_mask:0xf bank_mask:0xf bound_ctrl:1
	v_max_f32_e32 v17, v17, v17
	v_max_f32_e32 v16, v16, v17
	s_nop 1
	v_mov_b32_dpp v17, v16 row_mirror row_mask:0xf bank_mask:0xf bound_ctrl:1
	v_max_f32_e32 v17, v17, v17
	v_max_f32_e32 v16, v16, v17
	v_mov_b32_e32 v17, v16
	v_mov_b32_e32 v60, v16
	s_nop 1
	v_permlane16_swap_b32 v17, v60
	v_max_f32_e32 v16, v17, v60
	v_mov_b32_e32 v17, v16
	v_mov_b32_e32 v60, v16
	s_nop 1
	v_permlane32_swap_b32 v17, v60
	v_max_f32_e32 v16, v17, v60
	v_cmp_eq_f32_e32 vcc, v9, v16
	v_cmp_eq_f32_e64 s[28:29], v14, v16
	v_cmp_eq_f32_e64 s[2:3], v15, v16
	v_cmp_eq_f32_e64 s[48:49], v0, v16
	s_cbranch_vccz .LBB0_632
	s_ff1_i32_b64 s61, vcc
	s_cbranch_execz .LBB0_633
	s_branch .LBB0_639

.LBB0_639:
	s_and_b32 s2, s61, 63
	s_lshr_b32 s28, s61, 6
	s_cmp_lt_u32 s61, 64
	v_cmp_eq_u32_e32 vcc, s2, v22
	s_cselect_b64 s[2:3], -1, 0
	s_and_b64 s[2:3], s[2:3], vcc
	s_cmp_eq_u32 s28, 1
	v_cndmask_b32_e64 v9, v9, v26, s[2:3]
	s_cselect_b64 s[2:3], -1, 0
	s_and_b64 s[2:3], vcc, s[2:3]
	s_cmp_eq_u32 s28, 2
	v_cndmask_b32_e64 v14, v14, v26, s[2:3]
	s_cselect_b64 s[2:3], -1, 0
	s_and_b64 s[2:3], vcc, s[2:3]
	s_cmp_eq_u32 s28, 3
	v_cndmask_b32_e64 v15, v15, v26, s[2:3]
	s_cselect_b64 s[2:3], -1, 0
	s_and_b64 vcc, vcc, s[2:3]
	v_cndmask_b32_e32 v0, v0, v26, vcc
	v_max_f32_e32 v16, v0, v0
	v_max_f32_e32 v17, v15, v15
	v_max_f32_e32 v16, v17, v16
	v_max3_f32 v16, v9, v14, v16
	s_nop 1
	v_mov_b32_dpp v17, v16 quad_perm:[1,0,3,2] row_mask:0xf bank_mask:0xf bound_ctrl:1
	v_max_f32_e32 v17, v17, v17
	v_max_f32_e32 v16, v16, v17
	s_nop 1
	v_mov_b32_dpp v17, v16 quad_perm:[2,3,0,1] row_mask:0xf bank_mask:0xf bound_ctrl:1
	v_max_f32_e32 v17, v17, v17
	v_max_f32_e32 v16, v16, v17
	s_nop 1
	v_mov_b32_dpp v17, v16 row_half_mirror row_mask:0xf bank_mask:0xf bound_ctrl:1
	v_max_f32_e32 v17, v17, v17
	v_max_f32_e32 v16, v16, v17
	s_nop 1
	v_mov_b32_dpp v17, v16 row_mirror row_mask:0xf bank_mask:0xf bound_ctrl:1
	v_max_f32_e32 v17, v17, v17
	v_max_f32_e32 v16, v16, v17
	v_mov_b32_e32 v17, v16
	v_mov_b32_e32 v60, v16
	s_nop 1
	v_permlane16_swap_b32 v17, v60
	v_max_f32_e32 v16, v17, v60
	v_mov_b32_e32 v17, v16
	v_mov_b32_e32 v60, v16
	s_nop 1
	v_permlane32_swap_b32 v17, v60
	v_max_f32_e32 v16, v17, v60
	v_cmp_eq_f32_e32 vcc, v9, v16
	v_cmp_eq_f32_e64 s[28:29], v14, v16
	v_cmp_eq_f32_e64 s[2:3], v15, v16
	v_cmp_eq_f32_e64 s[48:49], v0, v16
	s_cbranch_vccz .LBB0_641
	s_ff1_i32_b64 s62, vcc
	s_cbranch_execz .LBB0_642
	s_branch .LBB0_648

.LBB0_648:
	s_and_b32 s2, s62, 63
	s_lshr_b32 s28, s62, 6
	s_cmp_lt_u32 s62, 64
	v_cmp_eq_u32_e32 vcc, s2, v22
	s_cselect_b64 s[2:3], -1, 0
	s_and_b64 s[2:3], s[2:3], vcc
	s_cmp_eq_u32 s28, 1
	v_cndmask_b32_e64 v9, v9, v26, s[2:3]
	s_cselect_b64 s[2:3], -1, 0
	s_and_b64 s[2:3], vcc, s[2:3]
	s_cmp_eq_u32 s28, 2
	v_cndmask_b32_e64 v14, v14, v26, s[2:3]
	s_cselect_b64 s[2:3], -1, 0
	s_and_b64 s[2:3], vcc, s[2:3]
	s_cmp_eq_u32 s28, 3
	v_cndmask_b32_e64 v15, v15, v26, s[2:3]
	s_cselect_b64 s[2:3], -1, 0
	s_and_b64 vcc, vcc, s[2:3]
	v_cndmask_b32_e32 v0, v0, v26, vcc
	v_max_f32_e32 v16, v0, v0
	v_max_f32_e32 v17, v15, v15
	v_max_f32_e32 v16, v17, v16
	v_max3_f32 v16, v9, v14, v16
	s_nop 1
	v_mov_b32_dpp v17, v16 quad_perm:[1,0,3,2] row_mask:0xf bank_mask:0xf bound_ctrl:1
	v_max_f32_e32 v17, v17, v17
	v_max_f32_e32 v16, v16, v17
	s_nop 1
	v_mov_b32_dpp v17, v16 quad_perm:[2,3,0,1] row_mask:0xf bank_mask:0xf bound_ctrl:1
	v_max_f32_e32 v17, v17, v17
	v_max_f32_e32 v16, v16, v17
	s_nop 1
	v_mov_b32_dpp v17, v16 row_half_mirror row_mask:0xf bank_mask:0xf bound_ctrl:1
	v_max_f32_e32 v17, v17, v17
	v_max_f32_e32 v16, v16, v17
	s_nop 1
	v_mov_b32_dpp v17, v16 row_mirror row_mask:0xf bank_mask:0xf bound_ctrl:1
	v_max_f32_e32 v17, v17, v17
	v_max_f32_e32 v16, v16, v17
	v_mov_b32_e32 v17, v16
	v_mov_b32_e32 v60, v16
	s_nop 1
	v_permlane16_swap_b32 v17, v60
	v_max_f32_e32 v16, v17, v60
	v_mov_b32_e32 v17, v16
	v_mov_b32_e32 v60, v16
	s_nop 1
	v_permlane32_swap_b32 v17, v60
	v_max_f32_e32 v16, v17, v60
	v_cmp_eq_f32_e32 vcc, v9, v16
	v_cmp_eq_f32_e64 s[28:29], v14, v16
	v_cmp_eq_f32_e64 s[2:3], v15, v16
	v_cmp_eq_f32_e64 s[48:49], v0, v16
	s_cbranch_vccz .LBB0_650
	s_ff1_i32_b64 s63, vcc
	s_cbranch_execz .LBB0_651
	s_branch .LBB0_657

.LBB0_2167:
	s_or_b64 exec, exec, s[28:29]
	v_cmp_gt_f32_e32 vcc, v0, v20
	v_cndmask_b32_e64 v18, 0, 1, s[26:27]
	s_nop 0
	v_cndmask_b32_e64 v0, 0, 1, vcc
	v_cmp_gt_f32_e32 vcc, v38, v20
	s_nop 1
	v_addc_co_u32_e32 v0, vcc, v0, v18, vcc
	v_cmp_gt_f32_e32 vcc, v9, v20
	s_nop 1
	v_cndmask_b32_e64 v9, 0, 1, vcc
	v_cmp_gt_f32_e32 vcc, v37, v20
	s_nop 1
	v_addc_co_u32_e32 v0, vcc, v0, v9, vcc
	v_cmp_gt_f32_e32 vcc, v39, v20
	s_nop 1
	v_cndmask_b32_e64 v9, 0, 1, vcc
	v_cmp_gt_f32_e32 vcc, v21, v20
	s_nop 1
	v_addc_co_u32_e32 v9, vcc, v0, v9, vcc
	v_mov_b32_e32 v0, s47
	v_cmp_gt_u32_e32 vcc, 4, v9
	s_nop 1
	v_cndmask_b32_e32 v9, v0, v14, vcc
	v_cndmask_b32_e32 v0, v17, v17, vcc
	v_cndmask_b32_e32 v16, v16, v16, vcc
	v_cndmask_b32_e32 v14, v15, v15, vcc
	v_cmp_gt_u32_e32 vcc, 4, v35
	s_nop 1
	v_cndmask_b32_e32 v14, v25, v14, vcc
	v_cmp_gt_u32_e32 vcc, 4, v34
	s_nop 1
	v_cndmask_b32_e32 v15, v25, v16, vcc
	v_cmp_gt_u32_e32 vcc, 4, v33
	v_max_f32_e32 v17, v15, v15
	s_nop 0
	v_cndmask_b32_e32 v0, v25, v0, vcc
	v_max_f32_e32 v16, v0, v0
	v_max_f32_e32 v16, v17, v16
	v_max3_f32 v16, v9, v14, v16
	s_nop 1
	v_mov_b32_dpp v17, v16 quad_perm:[1,0,3,2] row_mask:0xf bank_mask:0xf bound_ctrl:1
	v_max_f32_e32 v17, v17, v17
	v_max_f32_e32 v16, v16, v17
	s_nop 1
	v_mov_b32_dpp v17, v16 quad_perm:[2,3,0,1] row_mask:0xf bank_mask:0xf bound_ctrl:1
	v_max_f32_e32 v17, v17, v17
	v_max_f32_e32 v16, v16, v17
	s_nop 1
	v_mov_b32_dpp v17, v16 row_half_mirror row_mask:0xf bank_mask:0xf bound_ctrl:1
	v_max_f32_e32 v17, v17, v17
	v_max_f32_e32 v16, v16, v17
	s_nop 1
	v_mov_b32_dpp v17, v16 row_mirror row_mask:0xf bank_mask:0xf bound_ctrl:1
	v_max_f32_e32 v17, v17, v17
	v_max_f32_e32 v16, v16, v17
	v_mov_b32_e32 v17, v16
	v_mov_b32_e32 v60, v16
	s_nop 1
	v_permlane16_swap_b32 v17, v60
	v_max_f32_e32 v16, v17, v60
	v_mov_b32_e32 v17, v16
	v_mov_b32_e32 v60, v16
	s_nop 1
	v_permlane32_swap_b32 v17, v60
	v_max_f32_e32 v16, v17, v60
	v_cmp_eq_f32_e32 vcc, v9, v16
	v_cmp_eq_f32_e64 s[28:29], v14, v16
	v_cmp_eq_f32_e64 s[26:27], v15, v16
	v_cmp_eq_f32_e64 s[38:39], v0, v16
	s_cbranch_vccz .LBB0_2169
	s_ff1_i32_b64 s48, vcc
	s_cbranch_execz .LBB0_2170
	s_branch .LBB0_2176

.LBB0_2176:
	s_and_b32 s26, s48, 63
	s_lshr_b32 s28, s48, 6
	s_cmp_lt_u32 s48, 64
	v_cmp_eq_u32_e32 vcc, s26, v22
	s_cselect_b64 s[26:27], -1, 0
	s_and_b64 s[26:27], s[26:27], vcc
	s_cmp_eq_u32 s28, 1
	v_cndmask_b32_e64 v9, v9, v25, s[26:27]
	s_cselect_b64 s[26:27], -1, 0
	s_and_b64 s[26:27], vcc, s[26:27]
	s_cmp_eq_u32 s28, 2
	v_cndmask_b32_e64 v14, v14, v25, s[26:27]
	s_cselect_b64 s[26:27], -1, 0
	s_and_b64 s[26:27], vcc, s[26:27]
	s_cmp_eq_u32 s28, 3
	v_cndmask_b32_e64 v15, v15, v25, s[26:27]
	s_cselect_b64 s[26:27], -1, 0
	s_and_b64 vcc, vcc, s[26:27]
	v_cndmask_b32_e32 v0, v0, v25, vcc
	v_max_f32_e32 v16, v0, v0
	v_max_f32_e32 v17, v15, v15
	v_max_f32_e32 v16, v17, v16
	v_max3_f32 v16, v9, v14, v16
	s_nop 1
	v_mov_b32_dpp v17, v16 quad_perm:[1,0,3,2] row_mask:0xf bank_mask:0xf bound_ctrl:1
	v_max_f32_e32 v17, v17, v17
	v_max_f32_e32 v16, v16, v17
	s_nop 1
	v_mov_b32_dpp v17, v16 quad_perm:[2,3,0,1] row_mask:0xf bank_mask:0xf bound_ctrl:1
	v_max_f32_e32 v17, v17, v17
	v_max_f32_e32 v16, v16, v17
	s_nop 1
	v_mov_b32_dpp v17, v16 row_half_mirror row_mask:0xf bank_mask:0xf bound_ctrl:1
	v_max_f32_e32 v17, v17, v17
	v_max_f32_e32 v16, v16, v17
	s_nop 1
	v_mov_b32_dpp v17, v16 row_mirror row_mask:0xf bank_mask:0xf bound_ctrl:1
	v_max_f32_e32 v17, v17, v17
	v_max_f32_e32 v16, v16, v17
	v_mov_b32_e32 v17, v16
	v_mov_b32_e32 v60, v16
	s_nop 1
	v_permlane16_swap_b32 v17, v60
	v_max_f32_e32 v16, v17, v60
	v_mov_b32_e32 v17, v16
	v_mov_b32_e32 v60, v16
	s_nop 1
	v_permlane32_swap_b32 v17, v60
	v_max_f32_e32 v16, v17, v60
	v_cmp_eq_f32_e32 vcc, v9, v16
	v_cmp_eq_f32_e64 s[28:29], v14, v16
	v_cmp_eq_f32_e64 s[26:27], v15, v16
	v_cmp_eq_f32_e64 s[38:39], v0, v16
	s_cbranch_vccz .LBB0_2178
	s_ff1_i32_b64 s49, vcc
	s_cbranch_execz .LBB0_2179
	s_branch .LBB0_2185

.LBB0_2185:
	s_and_b32 s26, s49, 63
	s_lshr_b32 s28, s49, 6
	s_cmp_lt_u32 s49, 64
	v_cmp_eq_u32_e32 vcc, s26, v22
	s_cselect_b64 s[26:27], -1, 0
	s_and_b64 s[26:27], s[26:27], vcc
	s_cmp_eq_u32 s28, 1
	v_cndmask_b32_e64 v9, v9, v25, s[26:27]
	s_cselect_b64 s[26:27], -1, 0
	s_and_b64 s[26:27], vcc, s[26:27]
	s_cmp_eq_u32 s28, 2
	v_cndmask_b32_e64 v14, v14, v25, s[26:27]
	s_cselect_b64 s[26:27], -1, 0
	s_and_b64 s[26:27], vcc, s[26:27]
	s_cmp_eq_u32 s28, 3
	v_cndmask_b32_e64 v15, v15, v25, s[26:27]
	s_cselect_b64 s[26:27], -1, 0
	s_and_b64 vcc, vcc, s[26:27]
	v_cndmask_b32_e32 v0, v0, v25, vcc
	v_max_f32_e32 v16, v0, v0
	v_max_f32_e32 v17, v15, v15
	v_max_f32_e32 v16, v17, v16
	v_max3_f32 v16, v9, v14, v16
	s_nop 1
	v_mov_b32_dpp v17, v16 quad_perm:[1,0,3,2] row_mask:0xf bank_mask:0xf bound_ctrl:1
	v_max_f32_e32 v17, v17, v17
	v_max_f32_e32 v16, v16, v17
	s_nop 1
	v_mov_b32_dpp v17, v16 quad_perm:[2,3,0,1] row_mask:0xf bank_mask:0xf bound_ctrl:1
	v_max_f32_e32 v17, v17, v17
	v_max_f32_e32 v16, v16, v17
	s_nop 1
	v_mov_b32_dpp v17, v16 row_half_mirror row_mask:0xf bank_mask:0xf bound_ctrl:1
	v_max_f32_e32 v17, v17, v17
	v_max_f32_e32 v16, v16, v17
	s_nop 1
	v_mov_b32_dpp v17, v16 row_mirror row_mask:0xf bank_mask:0xf bound_ctrl:1
	v_max_f32_e32 v17, v17, v17
	v_max_f32_e32 v16, v16, v17
	v_mov_b32_e32 v17, v16
	v_mov_b32_e32 v60, v16
	s_nop 1
	v_permlane16_swap_b32 v17, v60
	v_max_f32_e32 v16, v17, v60
	v_mov_b32_e32 v17, v16
	v_mov_b32_e32 v60, v16
	s_nop 1
	v_permlane32_swap_b32 v17, v60
	v_max_f32_e32 v16, v17, v60
	v_cmp_eq_f32_e32 vcc, v9, v16
	v_cmp_eq_f32_e64 s[28:29], v14, v16
	v_cmp_eq_f32_e64 s[26:27], v15, v16
	v_cmp_eq_f32_e64 s[38:39], v0, v16
	s_cbranch_vccz .LBB0_2187
	s_ff1_i32_b64 s50, vcc
	s_cbranch_execz .LBB0_2188
	s_branch .LBB0_2194

.LBB0_2194:
	s_and_b32 s26, s50, 63
	s_lshr_b32 s28, s50, 6
	s_cmp_lt_u32 s50, 64
	v_cmp_eq_u32_e32 vcc, s26, v22
	s_cselect_b64 s[26:27], -1, 0
	s_and_b64 s[26:27], s[26:27], vcc
	s_cmp_eq_u32 s28, 1
	v_cndmask_b32_e64 v9, v9, v25, s[26:27]
	s_cselect_b64 s[26:27], -1, 0
	s_and_b64 s[26:27], vcc, s[26:27]
	s_cmp_eq_u32 s28, 2
	v_cndmask_b32_e64 v14, v14, v25, s[26:27]
	s_cselect_b64 s[26:27], -1, 0
	s_and_b64 s[26:27], vcc, s[26:27]
	s_cmp_eq_u32 s28, 3
	v_cndmask_b32_e64 v15, v15, v25, s[26:27]
	s_cselect_b64 s[26:27], -1, 0
	s_and_b64 vcc, vcc, s[26:27]
	v_cndmask_b32_e32 v0, v0, v25, vcc
	v_max_f32_e32 v16, v0, v0
	v_max_f32_e32 v17, v15, v15
	v_max_f32_e32 v16, v17, v16
	v_max3_f32 v16, v9, v14, v16
	s_nop 1
	v_mov_b32_dpp v17, v16 quad_perm:[1,0,3,2] row_mask:0xf bank_mask:0xf bound_ctrl:1
	v_max_f32_e32 v17, v17, v17
	v_max_f32_e32 v16, v16, v17
	s_nop 1
	v_mov_b32_dpp v17, v16 quad_perm:[2,3,0,1] row_mask:0xf bank_mask:0xf bound_ctrl:1
	v_max_f32_e32 v17, v17, v17
	v_max_f32_e32 v16, v16, v17
	s_nop 1
	v_mov_b32_dpp v17, v16 row_half_mirror row_mask:0xf bank_mask:0xf bound_ctrl:1
	v_max_f32_e32 v17, v17, v17
	v_max_f32_e32 v16, v16, v17
	s_nop 1
	v_mov_b32_dpp v17, v16 row_mirror row_mask:0xf bank_mask:0xf bound_ctrl:1
	v_max_f32_e32 v17, v17, v17
	v_max_f32_e32 v16, v16, v17
	v_mov_b32_e32 v17, v16
	v_mov_b32_e32 v60, v16
	s_nop 1
	v_permlane16_swap_b32 v17, v60
	v_max_f32_e32 v16, v17, v60
	v_mov_b32_e32 v17, v16
	v_mov_b32_e32 v60, v16
	s_nop 1
	v_permlane32_swap_b32 v17, v60
	v_max_f32_e32 v16, v17, v60
	v_cmp_eq_f32_e32 vcc, v9, v16
	v_cmp_eq_f32_e64 s[28:29], v14, v16
	v_cmp_eq_f32_e64 s[26:27], v15, v16
	v_cmp_eq_f32_e64 s[38:39], v0, v16
	s_cbranch_vccz .LBB0_2196
	s_ff1_i32_b64 s51, vcc
	s_cbranch_execz .LBB0_2197
	s_branch .LBB0_2203

.LBB0_2203:
	s_and_b32 s26, s51, 63
	s_lshr_b32 s28, s51, 6
	s_cmp_lt_u32 s51, 64
	v_cmp_eq_u32_e32 vcc, s26, v22
	s_cselect_b64 s[26:27], -1, 0
	s_and_b64 s[26:27], s[26:27], vcc
	s_cmp_eq_u32 s28, 1
	v_cndmask_b32_e64 v9, v9, v25, s[26:27]
	s_cselect_b64 s[26:27], -1, 0
	s_and_b64 s[26:27], vcc, s[26:27]
	s_cmp_eq_u32 s28, 2
	v_cndmask_b32_e64 v14, v14, v25, s[26:27]
	s_cselect_b64 s[26:27], -1, 0
	s_and_b64 s[26:27], vcc, s[26:27]
	s_cmp_eq_u32 s28, 3
	v_cndmask_b32_e64 v15, v15, v25, s[26:27]
	s_cselect_b64 s[26:27], -1, 0
	s_and_b64 vcc, vcc, s[26:27]
	v_cndmask_b32_e32 v0, v0, v25, vcc
	v_max_f32_e32 v16, v0, v0
	v_max_f32_e32 v17, v15, v15
	v_max_f32_e32 v16, v17, v16
	v_max3_f32 v16, v9, v14, v16
	s_nop 1
	v_mov_b32_dpp v17, v16 quad_perm:[1,0,3,2] row_mask:0xf bank_mask:0xf bound_ctrl:1
	v_max_f32_e32 v17, v17, v17
	v_max_f32_e32 v16, v16, v17
	s_nop 1
	v_mov_b32_dpp v17, v16 quad_perm:[2,3,0,1] row_mask:0xf bank_mask:0xf bound_ctrl:1
	v_max_f32_e32 v17, v17, v17
	v_max_f32_e32 v16, v16, v17
	s_nop 1
	v_mov_b32_dpp v17, v16 row_half_mirror row_mask:0xf bank_mask:0xf bound_ctrl:1
	v_max_f32_e32 v17, v17, v17
	v_max_f32_e32 v16, v16, v17
	s_nop 1
	v_mov_b32_dpp v17, v16 row_mirror row_mask:0xf bank_mask:0xf bound_ctrl:1
	v_max_f32_e32 v17, v17, v17
	v_max_f32_e32 v16, v16, v17
	v_mov_b32_e32 v17, v16
	v_mov_b32_e32 v60, v16
	s_nop 1
	v_permlane16_swap_b32 v17, v60
	v_max_f32_e32 v16, v17, v60
	v_mov_b32_e32 v17, v16
	v_mov_b32_e32 v60, v16
	s_nop 1
	v_permlane32_swap_b32 v17, v60
	v_max_f32_e32 v16, v17, v60
	v_cmp_eq_f32_e32 vcc, v9, v16
	v_cmp_eq_f32_e64 s[28:29], v14, v16
	v_cmp_eq_f32_e64 s[26:27], v15, v16
	v_cmp_eq_f32_e64 s[38:39], v0, v16
	s_cbranch_vccz .LBB0_2205
	s_ff1_i32_b64 s52, vcc
	s_cbranch_execz .LBB0_2206
	s_branch .LBB0_2212

.LBB0_2212:
	s_and_b32 s26, s52, 63
	s_lshr_b32 s28, s52, 6
	s_cmp_lt_u32 s52, 64
	v_cmp_eq_u32_e32 vcc, s26, v22
	s_cselect_b64 s[26:27], -1, 0
	s_and_b64 s[26:27], s[26:27], vcc
	s_cmp_eq_u32 s28, 1
	v_cndmask_b32_e64 v9, v9, v25, s[26:27]
	s_cselect_b64 s[26:27], -1, 0
	s_and_b64 s[26:27], vcc, s[26:27]
	s_cmp_eq_u32 s28, 2
	v_cndmask_b32_e64 v14, v14, v25, s[26:27]
	s_cselect_b64 s[26:27], -1, 0
	s_and_b64 s[26:27], vcc, s[26:27]
	s_cmp_eq_u32 s28, 3
	v_cndmask_b32_e64 v15, v15, v25, s[26:27]
	s_cselect_b64 s[26:27], -1, 0
	s_and_b64 vcc, vcc, s[26:27]
	v_cndmask_b32_e32 v0, v0, v25, vcc
	v_max_f32_e32 v16, v0, v0
	v_max_f32_e32 v17, v15, v15
	v_max_f32_e32 v16, v17, v16
	v_max3_f32 v16, v9, v14, v16
	s_nop 1
	v_mov_b32_dpp v17, v16 quad_perm:[1,0,3,2] row_mask:0xf bank_mask:0xf bound_ctrl:1
	v_max_f32_e32 v17, v17, v17
	v_max_f32_e32 v16, v16, v17
	s_nop 1
	v_mov_b32_dpp v17, v16 quad_perm:[2,3,0,1] row_mask:0xf bank_mask:0xf bound_ctrl:1
	v_max_f32_e32 v17, v17, v17
	v_max_f32_e32 v16, v16, v17
	s_nop 1
	v_mov_b32_dpp v17, v16 row_half_mirror row_mask:0xf bank_mask:0xf bound_ctrl:1
	v_max_f32_e32 v17, v17, v17
	v_max_f32_e32 v16, v16, v17
	s_nop 1
	v_mov_b32_dpp v17, v16 row_mirror row_mask:0xf bank_mask:0xf bound_ctrl:1
	v_max_f32_e32 v17, v17, v17
	v_max_f32_e32 v16, v16, v17
	v_mov_b32_e32 v17, v16
	v_mov_b32_e32 v60, v16
	s_nop 1
	v_permlane16_swap_b32 v17, v60
	v_max_f32_e32 v16, v17, v60
	v_mov_b32_e32 v17, v16
	v_mov_b32_e32 v60, v16
	s_nop 1
	v_permlane32_swap_b32 v17, v60
	v_max_f32_e32 v16, v17, v60
	v_cmp_eq_f32_e32 vcc, v9, v16
	v_cmp_eq_f32_e64 s[28:29], v14, v16
	v_cmp_eq_f32_e64 s[26:27], v15, v16
	v_cmp_eq_f32_e64 s[38:39], v0, v16
	s_cbranch_vccz .LBB0_2214
	s_ff1_i32_b64 s53, vcc
	s_cbranch_execz .LBB0_2215
	s_branch .LBB0_2221

.LBB0_2221:
	s_and_b32 s26, s53, 63
	s_lshr_b32 s28, s53, 6
	s_cmp_lt_u32 s53, 64
	v_cmp_eq_u32_e32 vcc, s26, v22
	s_cselect_b64 s[26:27], -1, 0
	s_and_b64 s[26:27], s[26:27], vcc
	s_cmp_eq_u32 s28, 1
	v_cndmask_b32_e64 v9, v9, v25, s[26:27]
	s_cselect_b64 s[26:27], -1, 0
	s_and_b64 s[26:27], vcc, s[26:27]
	s_cmp_eq_u32 s28, 2
	v_cndmask_b32_e64 v14, v14, v25, s[26:27]
	s_cselect_b64 s[26:27], -1, 0
	s_and_b64 s[26:27], vcc, s[26:27]
	s_cmp_eq_u32 s28, 3
	v_cndmask_b32_e64 v15, v15, v25, s[26:27]
	s_cselect_b64 s[26:27], -1, 0
	s_and_b64 vcc, vcc, s[26:27]
	v_cndmask_b32_e32 v0, v0, v25, vcc
	v_max_f32_e32 v16, v0, v0
	v_max_f32_e32 v17, v15, v15
	v_max_f32_e32 v16, v17, v16
	v_max3_f32 v16, v9, v14, v16
	s_nop 1
	v_mov_b32_dpp v17, v16 quad_perm:[1,0,3,2] row_mask:0xf bank_mask:0xf bound_ctrl:1
	v_max_f32_e32 v17, v17, v17
	v_max_f32_e32 v16, v16, v17
	s_nop 1
	v_mov_b32_dpp v17, v16 quad_perm:[2,3,0,1] row_mask:0xf bank_mask:0xf bound_ctrl:1
	v_max_f32_e32 v17, v17, v17
	v_max_f32_e32 v16, v16, v17
	s_nop 1
	v_mov_b32_dpp v17, v16 row_half_mirror row_mask:0xf bank_mask:0xf bound_ctrl:1
	v_max_f32_e32 v17, v17, v17
	v_max_f32_e32 v16, v16, v17
	s_nop 1
	v_mov_b32_dpp v17, v16 row_mirror row_mask:0xf bank_mask:0xf bound_ctrl:1
	v_max_f32_e32 v17, v17, v17
	v_max_f32_e32 v16, v16, v17
	v_mov_b32_e32 v17, v16
	v_mov_b32_e32 v60, v16
	s_nop 1
	v_permlane16_swap_b32 v17, v60
	v_max_f32_e32 v16, v17, v60
	v_mov_b32_e32 v17, v16
	v_mov_b32_e32 v60, v16
	s_nop 1
	v_permlane32_swap_b32 v17, v60
	v_max_f32_e32 v16, v17, v60
	v_cmp_eq_f32_e32 vcc, v9, v16
	v_cmp_eq_f32_e64 s[28:29], v14, v16
	v_cmp_eq_f32_e64 s[26:27], v15, v16
	v_cmp_eq_f32_e64 s[38:39], v0, v16
	s_cbranch_vccz .LBB0_2223
	s_ff1_i32_b64 s54, vcc
	s_cbranch_execz .LBB0_2224
	s_branch .LBB0_2230

.LBB0_2230:
	s_and_b32 s26, s54, 63
	s_lshr_b32 s28, s54, 6
	s_cmp_lt_u32 s54, 64
	v_cmp_eq_u32_e32 vcc, s26, v22
	s_cselect_b64 s[26:27], -1, 0
	s_and_b64 s[26:27], s[26:27], vcc
	s_cmp_eq_u32 s28, 1
	v_cndmask_b32_e64 v9, v9, v25, s[26:27]
	s_cselect_b64 s[26:27], -1, 0
	s_and_b64 s[26:27], vcc, s[26:27]
	s_cmp_eq_u32 s28, 2
	v_cndmask_b32_e64 v14, v14, v25, s[26:27]
	s_cselect_b64 s[26:27], -1, 0
	s_and_b64 s[26:27], vcc, s[26:27]
	s_cmp_eq_u32 s28, 3
	v_cndmask_b32_e64 v15, v15, v25, s[26:27]
	s_cselect_b64 s[26:27], -1, 0
	s_and_b64 vcc, vcc, s[26:27]
	v_cndmask_b32_e32 v0, v0, v25, vcc
	v_max_f32_e32 v16, v0, v0
	v_max_f32_e32 v17, v15, v15
	v_max_f32_e32 v16, v17, v16
	v_max3_f32 v16, v9, v14, v16
	s_nop 1
	v_mov_b32_dpp v17, v16 quad_perm:[1,0,3,2] row_mask:0xf bank_mask:0xf bound_ctrl:1
	v_max_f32_e32 v17, v17, v17
	v_max_f32_e32 v16, v16, v17
	s_nop 1
	v_mov_b32_dpp v17, v16 quad_perm:[2,3,0,1] row_mask:0xf bank_mask:0xf bound_ctrl:1
	v_max_f32_e32 v17, v17, v17
	v_max_f32_e32 v16, v16, v17
	s_nop 1
	v_mov_b32_dpp v17, v16 row_half_mirror row_mask:0xf bank_mask:0xf bound_ctrl:1
	v_max_f32_e32 v17, v17, v17
	v_max_f32_e32 v16, v16, v17
	s_nop 1
	v_mov_b32_dpp v17, v16 row_mirror row_mask:0xf bank_mask:0xf bound_ctrl:1
	v_max_f32_e32 v17, v17, v17
	v_max_f32_e32 v16, v16, v17
	v_mov_b32_e32 v17, v16
	v_mov_b32_e32 v60, v16
	s_nop 1
	v_permlane16_swap_b32 v17, v60
	v_max_f32_e32 v16, v17, v60
	v_mov_b32_e32 v17, v16
	v_mov_b32_e32 v60, v16
	s_nop 1
	v_permlane32_swap_b32 v17, v60
	v_max_f32_e32 v16, v17, v60
	v_cmp_eq_f32_e32 vcc, v9, v16
	v_cmp_eq_f32_e64 s[28:29], v14, v16
	v_cmp_eq_f32_e64 s[26:27], v15, v16
	v_cmp_eq_f32_e64 s[38:39], v0, v16
	s_cbranch_vccz .LBB0_2232
	s_ff1_i32_b64 s55, vcc
	s_cbranch_execz .LBB0_2233
	s_branch .LBB0_2239
